# gather: serpentine sweep - odd token rounds walk the sorted expert list downwards so early finishers rejoin the laggards' table window
# speedup vs baseline: 1.0012x; 1.0012x over previous
.LBB0_1405:
	s_barrier
	s_waitcnt vmcnt(12)
	v_mov_b32_e32 v18, v134
	v_mov_b32_e32 v16, v135
	v_mov_b32_e32 v19, v136
	v_mov_b32_e32 v17, v137
	s_ashr_i32 s45, s44, 31
	s_lshl_b64 s[0:1], s[44:45], 12
	v_lshl_add_u64 v[100:101], v[84:85], 0, s[0:1]
	v_lshl_add_u64 v[24:25], v[94:95], 0, s[0:1]
	global_load_dwordx4 v[0:3], v[100:101], off offset:48
	global_load_dwordx4 v[4:7], v[100:101], off offset:32
	global_load_dwordx4 v[8:11], v[100:101], off offset:16
	global_load_dwordx4 v[12:15], v[100:101], off
	global_load_dwordx4 v[32:35], v[24:25], off
	global_load_dwordx4 v[138:141], v[24:25], off offset:16
	global_load_dwordx4 v[206:209], v[24:25], off offset:32
	global_load_dwordx4 v[98:101], v[24:25], off offset:48
	s_add_i32 s1, s44, s38
	s_cmpk_lt_i32 s1, 0x4000
	s_cselect_b32 s1, s1, s44
	s_lshl_b32 s0, s1, 9
	v_lshl_add_u32 v26, v80, 2, s0
	global_load_dword v134, v26, s[46:47]
	global_load_dword v135, v26, s[46:47] offset:256
	global_load_dword v136, v26, s[48:49]
	global_load_dword v137, v26, s[48:49] offset:256
	v_lshrrev_b32_e32 v20, 10, v18
	v_lshrrev_b32_e32 v21, 10, v16
	v_mov_b32_e32 v24, 0
	v_cmp_eq_u32_e64 s[8:9], v20, 0
	v_cmp_eq_u32_e64 s[14:15], v21, 0
	s_bcnt1_i32_b64 s2, s[8:9]
	s_bcnt1_i32_b64 s4, s[14:15]
	v_mbcnt_lo_u32_b32 v25, s8, v24
	v_mbcnt_hi_u32_b32 v25, s9, v25
	v_add_u32_e32 v24, s2, v24
	v_cndmask_b32_e64 v22, v22, v25, s[8:9]
	v_mbcnt_lo_u32_b32 v26, s14, v24
	v_mbcnt_hi_u32_b32 v26, s15, v26
	v_add_u32_e32 v24, s4, v24
	v_cndmask_b32_e64 v23, v23, v26, s[14:15]
	v_cmp_eq_u32_e64 s[8:9], v20, 1
	v_cmp_eq_u32_e64 s[14:15], v21, 1
	s_bcnt1_i32_b64 s2, s[8:9]
	s_bcnt1_i32_b64 s4, s[14:15]
	v_mbcnt_lo_u32_b32 v25, s8, v24
	v_mbcnt_hi_u32_b32 v25, s9, v25
	v_add_u32_e32 v24, s2, v24
	v_cndmask_b32_e64 v22, v22, v25, s[8:9]
	v_mbcnt_lo_u32_b32 v26, s14, v24
	v_mbcnt_hi_u32_b32 v26, s15, v26
	v_add_u32_e32 v24, s4, v24
	v_cndmask_b32_e64 v23, v23, v26, s[14:15]
	v_cmp_eq_u32_e64 s[8:9], v20, 2
	v_cmp_eq_u32_e64 s[14:15], v21, 2
	s_bcnt1_i32_b64 s2, s[8:9]
	s_bcnt1_i32_b64 s4, s[14:15]
	v_mbcnt_lo_u32_b32 v25, s8, v24
	v_mbcnt_hi_u32_b32 v25, s9, v25
	v_add_u32_e32 v24, s2, v24
	v_cndmask_b32_e64 v22, v22, v25, s[8:9]
	v_mbcnt_lo_u32_b32 v26, s14, v24
	v_mbcnt_hi_u32_b32 v26, s15, v26
	v_add_u32_e32 v24, s4, v24
	v_cndmask_b32_e64 v23, v23, v26, s[14:15]
	v_cmp_eq_u32_e64 s[8:9], v20, 3
	v_cmp_eq_u32_e64 s[14:15], v21, 3
	s_bcnt1_i32_b64 s2, s[8:9]
	s_bcnt1_i32_b64 s4, s[14:15]
	v_mbcnt_lo_u32_b32 v25, s8, v24
	v_mbcnt_hi_u32_b32 v25, s9, v25
	v_add_u32_e32 v24, s2, v24
	v_cndmask_b32_e64 v22, v22, v25, s[8:9]
	v_mbcnt_lo_u32_b32 v26, s14, v24
	v_mbcnt_hi_u32_b32 v26, s15, v26
	v_add_u32_e32 v24, s4, v24
	v_cndmask_b32_e64 v23, v23, v26, s[14:15]
	v_cmp_eq_u32_e64 s[8:9], v20, 4
	v_cmp_eq_u32_e64 s[14:15], v21, 4
	s_bcnt1_i32_b64 s2, s[8:9]
	s_bcnt1_i32_b64 s4, s[14:15]
	v_mbcnt_lo_u32_b32 v25, s8, v24
	v_mbcnt_hi_u32_b32 v25, s9, v25
	v_add_u32_e32 v24, s2, v24
	v_cndmask_b32_e64 v22, v22, v25, s[8:9]
	v_mbcnt_lo_u32_b32 v26, s14, v24
	v_mbcnt_hi_u32_b32 v26, s15, v26
	v_add_u32_e32 v24, s4, v24
	v_cndmask_b32_e64 v23, v23, v26, s[14:15]
	v_cmp_eq_u32_e64 s[8:9], v20, 5
	v_cmp_eq_u32_e64 s[14:15], v21, 5
	s_bcnt1_i32_b64 s2, s[8:9]
	s_bcnt1_i32_b64 s4, s[14:15]
	v_mbcnt_lo_u32_b32 v25, s8, v24
	v_mbcnt_hi_u32_b32 v25, s9, v25
	v_add_u32_e32 v24, s2, v24
	v_cndmask_b32_e64 v22, v22, v25, s[8:9]
	v_mbcnt_lo_u32_b32 v26, s14, v24
	v_mbcnt_hi_u32_b32 v26, s15, v26
	v_add_u32_e32 v24, s4, v24
	v_cndmask_b32_e64 v23, v23, v26, s[14:15]
	v_cmp_eq_u32_e64 s[8:9], v20, 6
	v_cmp_eq_u32_e64 s[14:15], v21, 6
	s_bcnt1_i32_b64 s2, s[8:9]
	s_bcnt1_i32_b64 s4, s[14:15]
	v_mbcnt_lo_u32_b32 v25, s8, v24
	v_mbcnt_hi_u32_b32 v25, s9, v25
	v_add_u32_e32 v24, s2, v24
	v_cndmask_b32_e64 v22, v22, v25, s[8:9]
	v_mbcnt_lo_u32_b32 v26, s14, v24
	v_mbcnt_hi_u32_b32 v26, s15, v26
	v_add_u32_e32 v24, s4, v24
	v_cndmask_b32_e64 v23, v23, v26, s[14:15]
	v_cmp_eq_u32_e64 s[8:9], v20, 7
	v_cmp_eq_u32_e64 s[14:15], v21, 7
	s_bcnt1_i32_b64 s2, s[8:9]
	s_bcnt1_i32_b64 s4, s[14:15]
	v_mbcnt_lo_u32_b32 v25, s8, v24
	v_mbcnt_hi_u32_b32 v25, s9, v25
	v_add_u32_e32 v24, s2, v24
	v_cndmask_b32_e64 v22, v22, v25, s[8:9]
	v_mbcnt_lo_u32_b32 v26, s14, v24
	v_mbcnt_hi_u32_b32 v26, s15, v26
	v_add_u32_e32 v24, s4, v24
	v_cndmask_b32_e64 v23, v23, v26, s[14:15]
	v_cmp_eq_u32_e64 s[8:9], v20, 8
	v_cmp_eq_u32_e64 s[14:15], v21, 8
	s_bcnt1_i32_b64 s2, s[8:9]
	s_bcnt1_i32_b64 s4, s[14:15]
	v_mbcnt_lo_u32_b32 v25, s8, v24
	v_mbcnt_hi_u32_b32 v25, s9, v25
	v_add_u32_e32 v24, s2, v24
	v_cndmask_b32_e64 v22, v22, v25, s[8:9]
	v_mbcnt_lo_u32_b32 v26, s14, v24
	v_mbcnt_hi_u32_b32 v26, s15, v26
	v_add_u32_e32 v24, s4, v24
	v_cndmask_b32_e64 v23, v23, v26, s[14:15]
	v_cmp_eq_u32_e64 s[8:9], v20, 9
	v_cmp_eq_u32_e64 s[14:15], v21, 9
	s_bcnt1_i32_b64 s2, s[8:9]
	s_bcnt1_i32_b64 s4, s[14:15]
	v_mbcnt_lo_u32_b32 v25, s8, v24
	v_mbcnt_hi_u32_b32 v25, s9, v25
	v_add_u32_e32 v24, s2, v24
	v_cndmask_b32_e64 v22, v22, v25, s[8:9]
	v_mbcnt_lo_u32_b32 v26, s14, v24
	v_mbcnt_hi_u32_b32 v26, s15, v26
	v_add_u32_e32 v24, s4, v24
	v_cndmask_b32_e64 v23, v23, v26, s[14:15]
	v_cmp_eq_u32_e64 s[8:9], v20, 10
	v_cmp_eq_u32_e64 s[14:15], v21, 10
	s_bcnt1_i32_b64 s2, s[8:9]
	s_bcnt1_i32_b64 s4, s[14:15]
	v_mbcnt_lo_u32_b32 v25, s8, v24
	v_mbcnt_hi_u32_b32 v25, s9, v25
	v_add_u32_e32 v24, s2, v24
	v_cndmask_b32_e64 v22, v22, v25, s[8:9]
	v_mbcnt_lo_u32_b32 v26, s14, v24
	v_mbcnt_hi_u32_b32 v26, s15, v26
	v_add_u32_e32 v24, s4, v24
	v_cndmask_b32_e64 v23, v23, v26, s[14:15]
	v_cmp_eq_u32_e64 s[8:9], v20, 11
	v_cmp_eq_u32_e64 s[14:15], v21, 11
	s_bcnt1_i32_b64 s2, s[8:9]
	s_bcnt1_i32_b64 s4, s[14:15]
	v_mbcnt_lo_u32_b32 v25, s8, v24
	v_mbcnt_hi_u32_b32 v25, s9, v25
	v_add_u32_e32 v24, s2, v24
	v_cndmask_b32_e64 v22, v22, v25, s[8:9]
	v_mbcnt_lo_u32_b32 v26, s14, v24
	v_mbcnt_hi_u32_b32 v26, s15, v26
	v_add_u32_e32 v24, s4, v24
	v_cndmask_b32_e64 v23, v23, v26, s[14:15]
	v_cmp_eq_u32_e64 s[8:9], v20, 12
	v_cmp_eq_u32_e64 s[14:15], v21, 12
	s_bcnt1_i32_b64 s2, s[8:9]
	s_bcnt1_i32_b64 s4, s[14:15]
	v_mbcnt_lo_u32_b32 v25, s8, v24
	v_mbcnt_hi_u32_b32 v25, s9, v25
	v_add_u32_e32 v24, s2, v24
	v_cndmask_b32_e64 v22, v22, v25, s[8:9]
	v_mbcnt_lo_u32_b32 v26, s14, v24
	v_mbcnt_hi_u32_b32 v26, s15, v26
	v_add_u32_e32 v24, s4, v24
	v_cndmask_b32_e64 v23, v23, v26, s[14:15]
	v_cmp_eq_u32_e64 s[8:9], v20, 13
	v_cmp_eq_u32_e64 s[14:15], v21, 13
	s_bcnt1_i32_b64 s2, s[8:9]
	s_bcnt1_i32_b64 s4, s[14:15]
	v_mbcnt_lo_u32_b32 v25, s8, v24
	v_mbcnt_hi_u32_b32 v25, s9, v25
	v_add_u32_e32 v24, s2, v24
	v_cndmask_b32_e64 v22, v22, v25, s[8:9]
	v_mbcnt_lo_u32_b32 v26, s14, v24
	v_mbcnt_hi_u32_b32 v26, s15, v26
	v_add_u32_e32 v24, s4, v24
	v_cndmask_b32_e64 v23, v23, v26, s[14:15]
	v_cmp_eq_u32_e64 s[8:9], v20, 14
	v_cmp_eq_u32_e64 s[14:15], v21, 14
	s_bcnt1_i32_b64 s2, s[8:9]
	s_bcnt1_i32_b64 s4, s[14:15]
	v_mbcnt_lo_u32_b32 v25, s8, v24
	v_mbcnt_hi_u32_b32 v25, s9, v25
	v_add_u32_e32 v24, s2, v24
	v_cndmask_b32_e64 v22, v22, v25, s[8:9]
	v_mbcnt_lo_u32_b32 v26, s14, v24
	v_mbcnt_hi_u32_b32 v26, s15, v26
	v_add_u32_e32 v24, s4, v24
	v_cndmask_b32_e64 v23, v23, v26, s[14:15]
	v_cmp_eq_u32_e64 s[8:9], v20, 15
	v_cmp_eq_u32_e64 s[14:15], v21, 15
	s_bcnt1_i32_b64 s2, s[8:9]
	s_bcnt1_i32_b64 s4, s[14:15]
	v_mbcnt_lo_u32_b32 v25, s8, v24
	v_mbcnt_hi_u32_b32 v25, s9, v25
	v_add_u32_e32 v24, s2, v24
	v_cndmask_b32_e64 v22, v22, v25, s[8:9]
	v_mbcnt_lo_u32_b32 v26, s14, v24
	v_mbcnt_hi_u32_b32 v26, s15, v26
	v_add_u32_e32 v24, s4, v24
	v_cndmask_b32_e64 v23, v23, v26, s[14:15]
	s_bitcmp1_b32 s44, 11
	s_cselect_b32 s2, 127, 0
	v_xor_b32_e32 v22, s2, v22
	v_xor_b32_e32 v23, s2, v23
	v_lshl_add_u32 v250, v22, 3, s21
	v_lshl_add_u32 v251, v23, 3, s21
	ds_write_b64 v250, v[18:19] offset:1024
	ds_write_b64 v251, v[16:17] offset:1024
	v_and_b32_e32 v212, 7, v80
	v_lshl_add_u32 v212, v212, 3, s21
	v_add_u32_e32 v212, 0x400, v212
	v_lshrrev_b32_e32 v213, 4, v80
	v_bfe_u32 v250, v80, 3, 1
	v_lshl_add_u32 v213, v213, 1, v250
	v_lshl_add_u32 v213, v213, 3, s21
	v_add_u32_e32 v213, 0x404, v213
	ds_read_b32 v200, v212
	s_waitcnt vmcnt(8)
	v_lshlrev_b32_e32 v102, 16, v12
	v_and_b32_e32 v103, 0xffff0000, v12
	v_lshlrev_b32_e32 v104, 16, v13
	v_and_b32_e32 v105, 0xffff0000, v13
	v_lshlrev_b32_e32 v106, 16, v14
	v_and_b32_e32 v107, 0xffff0000, v14
	v_lshlrev_b32_e32 v108, 16, v15
	v_and_b32_e32 v109, 0xffff0000, v15
	v_lshlrev_b32_e32 v110, 16, v8
	v_and_b32_e32 v111, 0xffff0000, v8
	v_lshlrev_b32_e32 v112, 16, v9
	v_and_b32_e32 v113, 0xffff0000, v9
	v_lshlrev_b32_e32 v114, 16, v10
	v_and_b32_e32 v115, 0xffff0000, v10
	v_lshlrev_b32_e32 v116, 16, v11
	v_and_b32_e32 v117, 0xffff0000, v11
	v_lshlrev_b32_e32 v118, 16, v4
	v_and_b32_e32 v119, 0xffff0000, v4
	v_lshlrev_b32_e32 v120, 16, v5
	v_and_b32_e32 v121, 0xffff0000, v5
	v_lshlrev_b32_e32 v122, 16, v6
	v_and_b32_e32 v123, 0xffff0000, v6
	v_lshlrev_b32_e32 v124, 16, v7
	v_and_b32_e32 v125, 0xffff0000, v7
	v_lshlrev_b32_e32 v126, 16, v0
	v_and_b32_e32 v127, 0xffff0000, v0
	v_lshlrev_b32_e32 v128, 16, v1
	v_and_b32_e32 v129, 0xffff0000, v1
	v_lshlrev_b32_e32 v130, 16, v2
	v_and_b32_e32 v131, 0xffff0000, v2
	v_lshlrev_b32_e32 v132, 16, v3
	v_and_b32_e32 v133, 0xffff0000, v3
	v_mov_b32_e32 v178, 0
	v_mov_b32_e32 v179, 0
	v_mov_b32_e32 v184, 0
	v_mov_b32_e32 v185, 0
	v_mov_b32_e32 v182, 0
	v_mov_b32_e32 v183, 0
	v_mov_b32_e32 v180, 0
	v_mov_b32_e32 v181, 0
	v_mov_b32_e32 v176, 0
	v_mov_b32_e32 v177, 0
	v_mov_b32_e32 v174, 0
	v_mov_b32_e32 v175, 0
	v_mov_b32_e32 v160, 0
	v_mov_b32_e32 v161, 0
	v_mov_b32_e32 v158, 0
	v_mov_b32_e32 v159, 0
	v_mov_b32_e32 v156, 0
	v_mov_b32_e32 v157, 0
	v_mov_b32_e32 v154, 0
	v_mov_b32_e32 v155, 0
	v_mov_b32_e32 v152, 0
	v_mov_b32_e32 v153, 0
	v_mov_b32_e32 v150, 0
	v_mov_b32_e32 v151, 0
	v_mov_b32_e32 v148, 0
	v_mov_b32_e32 v149, 0
	v_mov_b32_e32 v146, 0
	v_mov_b32_e32 v147, 0
	v_mov_b32_e32 v144, 0
	v_mov_b32_e32 v145, 0
	v_mov_b32_e32 v142, 0
	v_mov_b32_e32 v143, 0
	s_waitcnt lgkmcnt(0)
	v_readlane_b32 s74, v200, 0
	s_lshl_b32 s24, s74, 10
	v_readlane_b32 s74, v200, 1
	s_lshl_b32 s28, s74, 10
	v_readlane_b32 s74, v200, 2
	s_lshl_b32 s29, s74, 10
	v_readlane_b32 s74, v200, 3
	s_lshl_b32 s34, s74, 10
	v_readlane_b32 s74, v200, 4
	s_lshl_b32 s35, s74, 10
	v_readlane_b32 s74, v200, 5
	s_lshl_b32 s42, s74, 10
	v_readlane_b32 s74, v200, 6
	s_lshl_b32 s43, s74, 10
	v_readlane_b32 s74, v200, 7
	s_lshl_b32 s50, s74, 10
	s_add_u32 s0, s93, s24
	s_addc_u32 s1, s20, 0
	global_load_dwordx4 v[0:3], v81, s[0:1]
	s_add_u32 s4, s93, s28
	s_addc_u32 s5, s20, 0
	global_load_dwordx4 v[4:7], v81, s[4:5]
	s_add_u32 s0, s93, s29
	s_addc_u32 s1, s20, 0
	global_load_dwordx4 v[8:11], v81, s[0:1]
	s_add_u32 s4, s93, s34
	s_addc_u32 s5, s20, 0
	global_load_dwordx4 v[12:15], v81, s[4:5]
	s_add_u32 s0, s93, s35
	s_addc_u32 s1, s20, 0
	global_load_dwordx4 v[16:19], v81, s[0:1]
	s_add_u32 s4, s93, s42
	s_addc_u32 s5, s20, 0
	global_load_dwordx4 v[20:23], v81, s[4:5]
	s_add_u32 s0, s93, s43
	s_addc_u32 s1, s20, 0
	global_load_dwordx4 v[24:27], v81, s[0:1]
	s_add_u32 s4, s93, s50
	s_addc_u32 s5, s20, 0
	global_load_dwordx4 v[28:31], v81, s[4:5]
	s_add_u32 s0, s89, s24
	s_addc_u32 s1, s92, 0
	global_load_dwordx4 v[36:39], v81, s[0:1]
	s_add_u32 s4, s89, s28
	s_addc_u32 s5, s92, 0
	global_load_dwordx4 v[40:43], v81, s[4:5]
	s_lshr_b32 s8, s24, 6
	s_add_u32 s8, s6, s8
	s_addc_u32 s9, s88, 0
	global_load_dword v68, v83, s[8:9]
	s_lshr_b32 s14, s28, 6
	s_add_u32 s14, s6, s14
	s_addc_u32 s15, s88, 0
	global_load_dword v69, v83, s[14:15]
	s_add_u32 s0, s89, s29
	s_addc_u32 s1, s92, 0
	global_load_dwordx4 v[44:47], v81, s[0:1]
	s_add_u32 s4, s89, s34
	s_addc_u32 s5, s92, 0
	global_load_dwordx4 v[48:51], v81, s[4:5]
	s_lshr_b32 s8, s29, 6
	s_add_u32 s8, s6, s8
	s_addc_u32 s9, s88, 0
	global_load_dword v70, v83, s[8:9]
	s_lshr_b32 s14, s34, 6
	s_add_u32 s14, s6, s14
	s_addc_u32 s15, s88, 0
	global_load_dword v71, v83, s[14:15]
	s_add_u32 s0, s89, s35
	s_addc_u32 s1, s92, 0
	global_load_dwordx4 v[52:55], v81, s[0:1]
	s_add_u32 s4, s89, s42
	s_addc_u32 s5, s92, 0
	global_load_dwordx4 v[56:59], v81, s[4:5]
	s_lshr_b32 s8, s35, 6
	s_add_u32 s8, s6, s8
	s_addc_u32 s9, s88, 0
	global_load_dword v72, v83, s[8:9]
	s_lshr_b32 s14, s42, 6
	s_add_u32 s14, s6, s14
	s_addc_u32 s15, s88, 0
	global_load_dword v73, v83, s[14:15]
	s_add_u32 s0, s89, s43
	s_addc_u32 s1, s92, 0
	global_load_dwordx4 v[60:63], v81, s[0:1]
	s_add_u32 s4, s89, s50
	s_addc_u32 s5, s92, 0
	global_load_dwordx4 v[64:67], v81, s[4:5]
	s_lshr_b32 s8, s43, 6
	s_add_u32 s8, s6, s8
	s_addc_u32 s9, s88, 0
	global_load_dword v74, v83, s[8:9]
	s_lshr_b32 s14, s50, 6
	s_add_u32 s14, s6, s14
	s_addc_u32 s15, s88, 0
	global_load_dword v75, v83, s[14:15]
	s_mov_b32 s2, 0
